# v30 = v28 with the RWKV-scan conversion loads at default cache policy (no nt)
# baseline (speedup 1.0000x reference)
; __device__ __forceinline__ ConvTile conv_tile_desc(const unsigned long long* tab, int t) {
;     ...
;     const int n0 = nb * 64;
;     int col0 = n0, nvalid = 64;
;     if (mode) { col0 = (n0 >> 8) * 128 + (n0 & 127); si += (n0 >> 7) & 1; }
;     if (npad) { nvalid = N - n0; if (nvalid <= 0) col0 = 0; }
;     ConvTile c;
;     const size_t KN = (size_t)K * N;
;     c.src = (const float*)tab[si] + (size_t)e * KN + (size_t)(kb * 32) * N + col0;
;     c.dst = (bf16_t*)tab[di] + (size_t)e * (mode ? 2 * KN : KN) + (size_t)n0 * K + kb * 32;
;     c.N = N; c.K = K; c.nvalid = nvalid;
;     return c;
; }
.LBB0_625:
	s_lshl_b32 s72, s33, 4
	s_lshl_b32 s33, s74, 6
	s_lshl_b32 s63, s74, 5
	s_and_b32 s63, s63, 0xffffff80
	s_and_b32 s75, s33, 64
	s_or_b32 s63, s63, s75
	s_bfe_u32 s78, s74, 0x10001
	s_and_b64 s[74:75], s[96:97], exec
	s_cselect_b32 s79, s33, s63
	s_cselect_b32 s63, 0, s78
	s_sub_i32 s33, s59, s33
	s_cmp_gt_i32 s33, 0
	s_cselect_b64 s[74:75], -1, 0
	s_lshl_b32 s64, s64, 3
	s_add_i32 s64, s64, 0
	s_lshl_b32 s63, s63, 3
	s_add_i32 s63, s64, s63
	s_add_i32 s63, s63, 0x20040
	v_mov_b32_e32 v58, s63
	ds_read_b64 v[58:59], v58
	s_mul_i32 s62, vcc_lo, s62
	s_mul_hi_u32 s63, s62, s59
	s_mul_i32 s62, s62, s59
	s_lshl_b64 s[62:63], s[62:63], 2
	s_waitcnt lgkmcnt(0)
	v_lshl_add_u64 v[58:59], v[58:59], 0, s[62:63]
	s_lshl_b32 s62, s65, 5
	s_mul_hi_i32 s63, s59, s62
	s_mul_i32 s62, s59, s62
	s_or_b64 s[74:75], s[60:61], s[74:75]
	s_lshl_b64 s[62:63], s[62:63], 2
	s_ashr_i32 s64, s79, 31
	v_lshl_add_u64 v[58:59], v[58:59], 0, s[62:63]
	s_and_b64 s[62:63], s[74:75], exec
	s_cselect_b32 s63, s64, 0
	s_cselect_b32 s62, s79, 0
	v_cmp_gt_i32_e32 vcc, s33, v136
	s_add_i32 s33, s59, s59
	s_lshl_b64 s[62:63], s[62:63], 2
	s_add_i32 s33, s33, s33
	v_lshl_add_u64 v[82:83], v[58:59], 0, s[62:63]
	v_mul_u32_u24_e32 v58, s59, v196
	v_mov_b32_e32 v74, s33
	v_lshlrev_b32_e32 v132, 2, v58
	s_or_b64 vcc, s[60:61], vcc
	v_mad_u32_u24 v76, s59, v196, v74
	v_lshl_add_u64 v[58:59], v[82:83], 0, v[132:133]
	v_cndmask_b32_e32 v60, 0, v136, vcc
	s_lshl_b32 s60, s59, 2
	s_mov_b32 s61, s73
	v_add_u32_e32 v84, s59, v76
	v_lshlrev_b32_e32 v132, 2, v60
	v_lshl_add_u64 v[66:67], v[58:59], 0, s[60:61]
	v_add_u32_e32 v86, s59, v84
	v_lshl_add_u64 v[62:63], v[66:67], 0, v[132:133]
	v_lshl_add_u64 v[66:67], v[66:67], 0, s[60:61]
	v_lshlrev_b32_e32 v74, 2, v76
	v_mov_b32_e32 v75, v133
	v_lshlrev_b32_e32 v76, 2, v84
	v_mov_b32_e32 v77, v133
	v_lshlrev_b32_e32 v84, 2, v86
	v_mov_b32_e32 v85, v133
	v_add_u32_e32 v86, s59, v86
	v_mov_b32_e32 v87, v133
	v_lshl_add_u64 v[68:69], v[66:67], 0, v[132:133]
	v_lshl_add_u64 v[66:67], v[66:67], 0, s[60:61]
	v_lshl_add_u64 v[74:75], v[82:83], 0, v[74:75]
	v_lshl_add_u64 v[76:77], v[82:83], 0, v[76:77]
	v_lshl_add_u64 v[84:85], v[82:83], 0, v[84:85]
	v_lshl_add_u64 v[82:83], v[86:87], 2, v[82:83]
	v_lshl_add_u64 v[60:61], v[58:59], 0, v[132:133]
	v_lshl_add_u64 v[70:71], v[66:67], 0, v[132:133]
	v_lshl_add_u64 v[74:75], v[74:75], 0, v[132:133]
	v_lshl_add_u64 v[78:79], v[76:77], 0, v[132:133]
	v_lshl_add_u64 v[84:85], v[84:85], 0, v[132:133]
	v_lshl_add_u64 v[86:87], v[82:83], 0, v[132:133]
	global_load_dwordx4 v[58:61], v[60:61], off
	s_nop 0
	global_load_dwordx4 v[62:65], v[62:63], off
	s_nop 0
	global_load_dwordx4 v[66:69], v[68:69], off
	s_nop 0
	global_load_dwordx4 v[70:73], v[70:71], off
	s_nop 0
	global_load_dwordx4 v[74:77], v[74:75], off
	s_nop 0
	global_load_dwordx4 v[78:81], v[78:79], off
	s_nop 0
	global_load_dwordx4 v[82:85], v[84:85], off
	s_nop 0
	global_load_dwordx4 v[86:89], v[86:87], off
	s_mov_b32 s59, s73
	s_movk_i32 s81, 0x100
	s_mov_b64 s[62:63], s[58:59]
	s_mov_b64 s[60:61], s[72:73]

; __device__ __forceinline__ ConvTile conv_tile_desc(const unsigned long long* tab, int t) {
;     ...
;     const int n0 = nb * 64;
;     int col0 = n0, nvalid = 64;
;     if (mode) { col0 = (n0 >> 8) * 128 + (n0 & 127); si += (n0 >> 7) & 1; }
;     if (npad) { nvalid = N - n0; if (nvalid <= 0) col0 = 0; }
;     ConvTile c;
;     const size_t KN = (size_t)K * N;
;     c.src = (const float*)tab[si] + (size_t)e * KN + (size_t)(kb * 32) * N + col0;
;     c.dst = (bf16_t*)tab[di] + (size_t)e * (mode ? 2 * KN : KN) + (size_t)n0 * K + kb * 32;
;     c.N = N; c.K = K; c.nvalid = nvalid;
;     return c;
; }
.LBB0_683:
	s_lshl_b32 s63, s75, 6
	s_lshl_b32 s65, s75, 5
	s_and_b32 s65, s65, 0xffffff80
	s_and_b32 s72, s63, 64
	s_or_b32 s65, s65, s72
	s_bfe_u32 s72, s75, 0x10001
	s_and_b64 s[60:61], s[60:61], exec
	s_cselect_b32 s65, s63, s65
	s_cselect_b32 s72, 0, s72
	s_sub_i32 s63, s56, s63
	s_cmp_gt_i32 s63, 0
	s_cselect_b64 s[60:61], -1, 0
	s_or_b64 s[60:61], s[58:59], s[60:61]
	s_and_b64 s[58:59], s[58:59], exec
	s_cselect_b32 s63, 64, s63
	s_lshl_b32 s57, s57, 3
	s_add_i32 s57, s57, 0
	s_lshl_b32 s58, s72, 3
	s_add_i32 s57, s57, s58
	s_add_i32 s57, s57, 0x20040
	v_mov_b32_e32 v58, s57
	ds_read_b64 v[58:59], v58
	s_mul_i32 s57, s62, s64
	s_mul_hi_u32 s59, s57, s56
	s_mul_i32 s58, s57, s56
	s_lshl_b64 s[58:59], s[58:59], 2
	s_lshl_b32 s57, s74, 5
	s_waitcnt lgkmcnt(0)
	v_lshl_add_u64 v[58:59], v[58:59], 0, s[58:59]
	s_ashr_i32 s58, s57, 31
	s_mul_i32 s58, s56, s58
	s_mul_hi_u32 s59, s56, s57
	s_add_i32 s59, s59, s58
	s_mul_i32 s58, s56, s57
	s_lshl_b64 s[58:59], s[58:59], 2
	s_ashr_i32 s57, s65, 31
	v_lshl_add_u64 v[58:59], v[58:59], 0, s[58:59]
	s_and_b64 s[58:59], s[60:61], exec
	s_cselect_b32 s59, s57, 0
	s_cselect_b32 s58, s65, 0
	s_lshl_b64 s[58:59], s[58:59], 2
	s_ashr_i32 s57, s56, 31
	v_lshl_add_u64 v[82:83], v[58:59], 0, s[58:59]
	s_lshl_b64 s[58:59], s[56:57], 2
	s_add_i32 s57, s56, s56
	v_mul_u32_u24_e32 v58, s56, v140
	v_cmp_gt_i32_e32 vcc, s63, v130
	s_add_i32 s57, s57, s56
	v_lshlrev_b32_e32 v132, 2, v58
	v_cndmask_b32_e32 v60, 0, v130, vcc
	v_mov_b32_e32 v74, s57
	v_lshl_add_u64 v[58:59], v[82:83], 0, v[132:133]
	v_lshlrev_b32_e32 v132, 2, v60
	v_mul_u32_u24_e32 v60, s56, v199
	v_mad_u32_u24 v74, s56, v199, v74
	v_lshlrev_b32_e32 v60, 2, v60
	v_mov_b32_e32 v61, v133
	v_mov_b32_e32 v75, v133
	v_add_u32_e32 v84, s56, v74
	v_mov_b32_e32 v85, v133
	v_lshl_add_u64 v[66:67], v[82:83], 0, v[60:61]
	v_lshl_add_u64 v[76:77], v[74:75], 2, v[82:83]
	v_lshl_add_u64 v[74:75], v[84:85], 2, v[82:83]
	v_add_u32_e32 v84, s56, v84
	v_lshl_add_u64 v[62:63], v[66:67], 0, v[132:133]
	v_lshl_add_u64 v[66:67], v[66:67], 0, s[58:59]
	v_lshl_add_u64 v[86:87], v[84:85], 2, v[82:83]
	v_add_u32_e32 v84, s56, v84
	v_lshl_add_u64 v[68:69], v[66:67], 0, v[132:133]
	v_lshl_add_u64 v[66:67], v[66:67], 0, s[58:59]
	v_lshl_add_u64 v[82:83], v[84:85], 2, v[82:83]
	v_lshl_add_u64 v[58:59], v[58:59], 0, v[132:133]
	v_lshl_add_u64 v[70:71], v[66:67], 0, v[132:133]
	v_lshl_add_u64 v[76:77], v[76:77], 0, v[132:133]
	v_lshl_add_u64 v[78:79], v[74:75], 0, v[132:133]
	v_lshl_add_u64 v[86:87], v[86:87], 0, v[132:133]
	v_lshl_add_u64 v[88:89], v[82:83], 0, v[132:133]
	global_load_dwordx4 v[58:61], v[58:59], off
	s_nop 0
	global_load_dwordx4 v[62:65], v[62:63], off
	s_nop 0
	global_load_dwordx4 v[66:69], v[68:69], off
	s_nop 0
	global_load_dwordx4 v[70:73], v[70:71], off
	s_nop 0
	global_load_dwordx4 v[74:77], v[76:77], off
	s_nop 0
	global_load_dwordx4 v[78:81], v[78:79], off
	s_nop 0
	global_load_dwordx4 v[82:85], v[86:87], off
	s_nop 0
	global_load_dwordx4 v[86:89], v[88:89], off
	s_mov_b64 s[96:97], s[76:77]
	s_branch .LBB0_685
